# SwiGLU fp8 epilogue of FFN and MoE gate/up rewritten: direct rcp per element (no pair trick, clamp, dead zero-inits, s_nop 32), in-place on dead accumulators; plus all-GEMM K-loop peel
# speedup vs baseline: 1.0307x; 1.0194x over previous
.LBB0_714:
	v_pk_mul_f32 v[16:17], v[158:159], s[20:21] op_sel_hi:[1,0]
	v_pk_mul_f32 v[18:19], v[160:161], s[20:21] op_sel_hi:[1,0]
	v_pk_mul_f32 v[20:21], v[150:151], s[20:21] op_sel_hi:[1,0]
	v_pk_mul_f32 v[22:23], v[152:153], s[20:21] op_sel_hi:[1,0]
	v_exp_f32_e32 v16, v16
	v_exp_f32_e32 v17, v17
	v_exp_f32_e32 v18, v18
	v_exp_f32_e32 v19, v19
	v_exp_f32_e32 v20, v20
	v_exp_f32_e32 v21, v21
	v_exp_f32_e32 v22, v22
	v_exp_f32_e32 v23, v23
	v_pk_add_f32 v[16:17], v[16:17], 1.0 op_sel_hi:[1,0]
	v_pk_add_f32 v[18:19], v[18:19], 1.0 op_sel_hi:[1,0]
	v_pk_add_f32 v[20:21], v[20:21], 1.0 op_sel_hi:[1,0]
	v_pk_add_f32 v[22:23], v[22:23], 1.0 op_sel_hi:[1,0]
	v_rcp_f32_e32 v16, v16
	v_rcp_f32_e32 v17, v17
	v_rcp_f32_e32 v18, v18
	v_rcp_f32_e32 v19, v19
	v_rcp_f32_e32 v20, v20
	v_rcp_f32_e32 v21, v21
	v_rcp_f32_e32 v22, v22
	v_rcp_f32_e32 v23, v23
	v_pk_mul_f32 v[158:159], v[158:159], v[154:155]
	v_pk_mul_f32 v[160:161], v[160:161], v[156:157]
	v_pk_mul_f32 v[150:151], v[150:151], v[146:147]
	v_pk_mul_f32 v[152:153], v[152:153], v[148:149]
	v_pk_mul_f32 v[158:159], v[158:159], v[16:17]
	v_pk_mul_f32 v[160:161], v[160:161], v[18:19]
	v_pk_mul_f32 v[150:151], v[150:151], v[20:21]
	v_pk_mul_f32 v[152:153], v[152:153], v[22:23]
	v_cvt_pk_fp8_f32 v8, v158, v159
	v_cvt_pk_fp8_f32 v9, v150, v151
	v_cvt_pk_fp8_f32 v8, v160, v161 op_sel:[0,0,1]
	v_cvt_pk_fp8_f32 v9, v152, v153 op_sel:[0,0,1]
	v_pk_mul_f32 v[16:17], v[142:143], s[20:21] op_sel_hi:[1,0]
	v_pk_mul_f32 v[18:19], v[144:145], s[20:21] op_sel_hi:[1,0]
	v_pk_mul_f32 v[20:21], v[134:135], s[20:21] op_sel_hi:[1,0]
	v_pk_mul_f32 v[22:23], v[136:137], s[20:21] op_sel_hi:[1,0]
	v_exp_f32_e32 v16, v16
	v_exp_f32_e32 v17, v17
	v_exp_f32_e32 v18, v18
	v_exp_f32_e32 v19, v19
	v_exp_f32_e32 v20, v20
	v_exp_f32_e32 v21, v21
	v_exp_f32_e32 v22, v22
	v_exp_f32_e32 v23, v23
	v_pk_add_f32 v[16:17], v[16:17], 1.0 op_sel_hi:[1,0]
	v_pk_add_f32 v[18:19], v[18:19], 1.0 op_sel_hi:[1,0]
	v_pk_add_f32 v[20:21], v[20:21], 1.0 op_sel_hi:[1,0]
	v_pk_add_f32 v[22:23], v[22:23], 1.0 op_sel_hi:[1,0]
	v_rcp_f32_e32 v16, v16
	v_rcp_f32_e32 v17, v17
	v_rcp_f32_e32 v18, v18
	v_rcp_f32_e32 v19, v19
	v_rcp_f32_e32 v20, v20
	v_rcp_f32_e32 v21, v21
	v_rcp_f32_e32 v22, v22
	v_rcp_f32_e32 v23, v23
	v_pk_mul_f32 v[142:143], v[142:143], v[138:139]
	v_pk_mul_f32 v[144:145], v[144:145], v[140:141]
	v_pk_mul_f32 v[134:135], v[134:135], v[130:131]
	v_pk_mul_f32 v[136:137], v[136:137], v[132:133]
	v_pk_mul_f32 v[142:143], v[142:143], v[16:17]
	v_pk_mul_f32 v[144:145], v[144:145], v[18:19]
	v_pk_mul_f32 v[134:135], v[134:135], v[20:21]
	v_pk_mul_f32 v[136:137], v[136:137], v[22:23]
	v_cvt_pk_fp8_f32 v10, v142, v143
	v_cvt_pk_fp8_f32 v11, v134, v135
	v_cvt_pk_fp8_f32 v10, v144, v145 op_sel:[0,0,1]
	v_cvt_pk_fp8_f32 v11, v136, v137 op_sel:[0,0,1]
	v_lshl_or_b32 v2, s78, 7, v191
	v_lshl_add_u32 v6, s44, 8, v190
	v_mov_b64_e32 v[4:5], s[8:9]
	v_ashrrev_i32_e32 v3, 31, v2
	v_mad_i64_i32 v[14:15], s[46:47], v6, s77, v[4:5]
	v_permlane16_swap_b32_e32 v8, v10
	v_permlane16_swap_b32_e32 v9, v11
	v_lshl_add_u64 v[14:15], v[14:15], 0, v[2:3]
	global_store_dwordx4 v[14:15], v[8:11], off
	v_pk_mul_f32 v[16:17], v[126:127], s[20:21] op_sel_hi:[1,0]
	v_pk_mul_f32 v[18:19], v[128:129], s[20:21] op_sel_hi:[1,0]
	v_pk_mul_f32 v[20:21], v[118:119], s[20:21] op_sel_hi:[1,0]
	v_pk_mul_f32 v[22:23], v[120:121], s[20:21] op_sel_hi:[1,0]
	v_exp_f32_e32 v16, v16
	v_exp_f32_e32 v17, v17
	v_exp_f32_e32 v18, v18
	v_exp_f32_e32 v19, v19
	v_exp_f32_e32 v20, v20
	v_exp_f32_e32 v21, v21
	v_exp_f32_e32 v22, v22
	v_exp_f32_e32 v23, v23
	v_pk_add_f32 v[16:17], v[16:17], 1.0 op_sel_hi:[1,0]
	v_pk_add_f32 v[18:19], v[18:19], 1.0 op_sel_hi:[1,0]
	v_pk_add_f32 v[20:21], v[20:21], 1.0 op_sel_hi:[1,0]
	v_pk_add_f32 v[22:23], v[22:23], 1.0 op_sel_hi:[1,0]
	v_rcp_f32_e32 v16, v16
	v_rcp_f32_e32 v17, v17
	v_rcp_f32_e32 v18, v18
	v_rcp_f32_e32 v19, v19
	v_rcp_f32_e32 v20, v20
	v_rcp_f32_e32 v21, v21
	v_rcp_f32_e32 v22, v22
	v_rcp_f32_e32 v23, v23
	v_pk_mul_f32 v[126:127], v[126:127], v[122:123]
	v_pk_mul_f32 v[128:129], v[128:129], v[124:125]
	v_pk_mul_f32 v[118:119], v[118:119], v[114:115]
	v_pk_mul_f32 v[120:121], v[120:121], v[116:117]
	v_pk_mul_f32 v[126:127], v[126:127], v[16:17]
	v_pk_mul_f32 v[128:129], v[128:129], v[18:19]
	v_pk_mul_f32 v[118:119], v[118:119], v[20:21]
	v_pk_mul_f32 v[120:121], v[120:121], v[22:23]
	v_cvt_pk_fp8_f32 v8, v126, v127
	v_cvt_pk_fp8_f32 v9, v118, v119
	v_cvt_pk_fp8_f32 v8, v128, v129 op_sel:[0,0,1]
	v_cvt_pk_fp8_f32 v9, v120, v121 op_sel:[0,0,1]
	v_pk_mul_f32 v[16:17], v[110:111], s[20:21] op_sel_hi:[1,0]
	v_pk_mul_f32 v[18:19], v[112:113], s[20:21] op_sel_hi:[1,0]
	v_pk_mul_f32 v[20:21], v[102:103], s[20:21] op_sel_hi:[1,0]
	v_pk_mul_f32 v[22:23], v[104:105], s[20:21] op_sel_hi:[1,0]
	v_exp_f32_e32 v16, v16
	v_exp_f32_e32 v17, v17
	v_exp_f32_e32 v18, v18
	v_exp_f32_e32 v19, v19
	v_exp_f32_e32 v20, v20
	v_exp_f32_e32 v21, v21
	v_exp_f32_e32 v22, v22
	v_exp_f32_e32 v23, v23
	v_pk_add_f32 v[16:17], v[16:17], 1.0 op_sel_hi:[1,0]
	v_pk_add_f32 v[18:19], v[18:19], 1.0 op_sel_hi:[1,0]
	v_pk_add_f32 v[20:21], v[20:21], 1.0 op_sel_hi:[1,0]
	v_pk_add_f32 v[22:23], v[22:23], 1.0 op_sel_hi:[1,0]
	v_rcp_f32_e32 v16, v16
	v_rcp_f32_e32 v17, v17
	v_rcp_f32_e32 v18, v18
	v_rcp_f32_e32 v19, v19
	v_rcp_f32_e32 v20, v20
	v_rcp_f32_e32 v21, v21
	v_rcp_f32_e32 v22, v22
	v_rcp_f32_e32 v23, v23
	v_pk_mul_f32 v[110:111], v[110:111], v[106:107]
	v_pk_mul_f32 v[112:113], v[112:113], v[108:109]
	v_pk_mul_f32 v[102:103], v[102:103], v[98:99]
	v_pk_mul_f32 v[104:105], v[104:105], v[100:101]
	v_pk_mul_f32 v[110:111], v[110:111], v[16:17]
	v_pk_mul_f32 v[112:113], v[112:113], v[18:19]
	v_pk_mul_f32 v[102:103], v[102:103], v[20:21]
	v_pk_mul_f32 v[104:105], v[104:105], v[22:23]
	v_cvt_pk_fp8_f32 v10, v110, v111
	v_cvt_pk_fp8_f32 v11, v102, v103
	v_cvt_pk_fp8_f32 v10, v112, v113 op_sel:[0,0,1]
	v_cvt_pk_fp8_f32 v11, v104, v105 op_sel:[0,0,1]
	v_or_b32_e32 v7, 32, v6
	v_mad_i64_i32 v[12:13], s[46:47], v7, s77, v[4:5]
	v_permlane16_swap_b32_e32 v8, v10
	v_permlane16_swap_b32_e32 v9, v11
	v_lshl_add_u64 v[12:13], v[12:13], 0, v[2:3]
	global_store_dwordx4 v[12:13], v[8:11], off
	v_pk_mul_f32 v[16:17], v[94:95], s[20:21] op_sel_hi:[1,0]
	v_pk_mul_f32 v[18:19], v[96:97], s[20:21] op_sel_hi:[1,0]
	v_pk_mul_f32 v[20:21], v[86:87], s[20:21] op_sel_hi:[1,0]
	v_pk_mul_f32 v[22:23], v[88:89], s[20:21] op_sel_hi:[1,0]
	v_exp_f32_e32 v16, v16
	v_exp_f32_e32 v17, v17
	v_exp_f32_e32 v18, v18
	v_exp_f32_e32 v19, v19
	v_exp_f32_e32 v20, v20
	v_exp_f32_e32 v21, v21
	v_exp_f32_e32 v22, v22
	v_exp_f32_e32 v23, v23
	v_pk_add_f32 v[16:17], v[16:17], 1.0 op_sel_hi:[1,0]
	v_pk_add_f32 v[18:19], v[18:19], 1.0 op_sel_hi:[1,0]
	v_pk_add_f32 v[20:21], v[20:21], 1.0 op_sel_hi:[1,0]
	v_pk_add_f32 v[22:23], v[22:23], 1.0 op_sel_hi:[1,0]
	v_rcp_f32_e32 v16, v16
	v_rcp_f32_e32 v17, v17
	v_rcp_f32_e32 v18, v18
	v_rcp_f32_e32 v19, v19
	v_rcp_f32_e32 v20, v20
	v_rcp_f32_e32 v21, v21
	v_rcp_f32_e32 v22, v22
	v_rcp_f32_e32 v23, v23
	v_pk_mul_f32 v[94:95], v[94:95], v[90:91]
	v_pk_mul_f32 v[96:97], v[96:97], v[92:93]
	v_pk_mul_f32 v[86:87], v[86:87], v[82:83]
	v_pk_mul_f32 v[88:89], v[88:89], v[84:85]
	v_pk_mul_f32 v[94:95], v[94:95], v[16:17]
	v_pk_mul_f32 v[96:97], v[96:97], v[18:19]
	v_pk_mul_f32 v[86:87], v[86:87], v[20:21]
	v_pk_mul_f32 v[88:89], v[88:89], v[22:23]
	v_cvt_pk_fp8_f32 v8, v94, v95
	v_cvt_pk_fp8_f32 v9, v86, v87
	v_cvt_pk_fp8_f32 v8, v96, v97 op_sel:[0,0,1]
	v_cvt_pk_fp8_f32 v9, v88, v89 op_sel:[0,0,1]
	v_pk_mul_f32 v[16:17], v[78:79], s[20:21] op_sel_hi:[1,0]
	v_pk_mul_f32 v[18:19], v[80:81], s[20:21] op_sel_hi:[1,0]
	v_pk_mul_f32 v[20:21], v[70:71], s[20:21] op_sel_hi:[1,0]
	v_pk_mul_f32 v[22:23], v[72:73], s[20:21] op_sel_hi:[1,0]
	v_exp_f32_e32 v16, v16
	v_exp_f32_e32 v17, v17
	v_exp_f32_e32 v18, v18
	v_exp_f32_e32 v19, v19
	v_exp_f32_e32 v20, v20
	v_exp_f32_e32 v21, v21
	v_exp_f32_e32 v22, v22
	v_exp_f32_e32 v23, v23
	v_pk_add_f32 v[16:17], v[16:17], 1.0 op_sel_hi:[1,0]
	v_pk_add_f32 v[18:19], v[18:19], 1.0 op_sel_hi:[1,0]
	v_pk_add_f32 v[20:21], v[20:21], 1.0 op_sel_hi:[1,0]
	v_pk_add_f32 v[22:23], v[22:23], 1.0 op_sel_hi:[1,0]
	v_rcp_f32_e32 v16, v16
	v_rcp_f32_e32 v17, v17
	v_rcp_f32_e32 v18, v18
	v_rcp_f32_e32 v19, v19
	v_rcp_f32_e32 v20, v20
	v_rcp_f32_e32 v21, v21
	v_rcp_f32_e32 v22, v22
	v_rcp_f32_e32 v23, v23
	v_pk_mul_f32 v[78:79], v[78:79], v[74:75]
	v_pk_mul_f32 v[80:81], v[80:81], v[76:77]
	v_pk_mul_f32 v[70:71], v[70:71], v[66:67]
	v_pk_mul_f32 v[72:73], v[72:73], v[68:69]
	v_pk_mul_f32 v[78:79], v[78:79], v[16:17]
	v_pk_mul_f32 v[80:81], v[80:81], v[18:19]
	v_pk_mul_f32 v[70:71], v[70:71], v[20:21]
	v_pk_mul_f32 v[72:73], v[72:73], v[22:23]
	v_cvt_pk_fp8_f32 v10, v78, v79
	v_cvt_pk_fp8_f32 v11, v70, v71
	v_cvt_pk_fp8_f32 v10, v80, v81 op_sel:[0,0,1]
	v_cvt_pk_fp8_f32 v11, v72, v73 op_sel:[0,0,1]
	v_add_u32_e32 v7, 0x80, v6
	v_mad_i64_i32 v[12:13], s[46:47], v7, s77, v[4:5]
	v_permlane16_swap_b32_e32 v8, v10
	v_permlane16_swap_b32_e32 v9, v11
	v_lshl_add_u64 v[12:13], v[12:13], 0, v[2:3]
	global_store_dwordx4 v[12:13], v[8:11], off
	v_pk_mul_f32 v[16:17], v[62:63], s[20:21] op_sel_hi:[1,0]
	v_pk_mul_f32 v[18:19], v[64:65], s[20:21] op_sel_hi:[1,0]
	v_pk_mul_f32 v[20:21], v[54:55], s[20:21] op_sel_hi:[1,0]
	v_pk_mul_f32 v[22:23], v[56:57], s[20:21] op_sel_hi:[1,0]
	v_exp_f32_e32 v16, v16
	v_exp_f32_e32 v17, v17
	v_exp_f32_e32 v18, v18
	v_exp_f32_e32 v19, v19
	v_exp_f32_e32 v20, v20
	v_exp_f32_e32 v21, v21
	v_exp_f32_e32 v22, v22
	v_exp_f32_e32 v23, v23
	v_pk_add_f32 v[16:17], v[16:17], 1.0 op_sel_hi:[1,0]
	v_pk_add_f32 v[18:19], v[18:19], 1.0 op_sel_hi:[1,0]
	v_pk_add_f32 v[20:21], v[20:21], 1.0 op_sel_hi:[1,0]
	v_pk_add_f32 v[22:23], v[22:23], 1.0 op_sel_hi:[1,0]
	v_rcp_f32_e32 v16, v16
	v_rcp_f32_e32 v17, v17
	v_rcp_f32_e32 v18, v18
	v_rcp_f32_e32 v19, v19
	v_rcp_f32_e32 v20, v20
	v_rcp_f32_e32 v21, v21
	v_rcp_f32_e32 v22, v22
	v_rcp_f32_e32 v23, v23
	v_pk_mul_f32 v[62:63], v[62:63], v[58:59]
	v_pk_mul_f32 v[64:65], v[64:65], v[60:61]
	v_pk_mul_f32 v[54:55], v[54:55], v[50:51]
	v_pk_mul_f32 v[56:57], v[56:57], v[52:53]
	v_pk_mul_f32 v[62:63], v[62:63], v[16:17]
	v_pk_mul_f32 v[64:65], v[64:65], v[18:19]
	v_pk_mul_f32 v[54:55], v[54:55], v[20:21]
	v_pk_mul_f32 v[56:57], v[56:57], v[22:23]
	v_cvt_pk_fp8_f32 v8, v62, v63
	v_cvt_pk_fp8_f32 v9, v54, v55
	v_cvt_pk_fp8_f32 v8, v64, v65 op_sel:[0,0,1]
	v_cvt_pk_fp8_f32 v9, v56, v57 op_sel:[0,0,1]
	v_pk_mul_f32 v[16:17], v[46:47], s[20:21] op_sel_hi:[1,0]
	v_pk_mul_f32 v[18:19], v[48:49], s[20:21] op_sel_hi:[1,0]
	v_pk_mul_f32 v[20:21], v[38:39], s[20:21] op_sel_hi:[1,0]
	v_pk_mul_f32 v[22:23], v[40:41], s[20:21] op_sel_hi:[1,0]
	v_exp_f32_e32 v16, v16
	v_exp_f32_e32 v17, v17
	v_exp_f32_e32 v18, v18
	v_exp_f32_e32 v19, v19
	v_exp_f32_e32 v20, v20
	v_exp_f32_e32 v21, v21
	v_exp_f32_e32 v22, v22
	v_exp_f32_e32 v23, v23
	v_pk_add_f32 v[16:17], v[16:17], 1.0 op_sel_hi:[1,0]
	v_pk_add_f32 v[18:19], v[18:19], 1.0 op_sel_hi:[1,0]
	v_pk_add_f32 v[20:21], v[20:21], 1.0 op_sel_hi:[1,0]
	v_pk_add_f32 v[22:23], v[22:23], 1.0 op_sel_hi:[1,0]
	v_rcp_f32_e32 v16, v16
	v_rcp_f32_e32 v17, v17
	v_rcp_f32_e32 v18, v18
	v_rcp_f32_e32 v19, v19
	v_rcp_f32_e32 v20, v20
	v_rcp_f32_e32 v21, v21
	v_rcp_f32_e32 v22, v22
	v_rcp_f32_e32 v23, v23
	v_pk_mul_f32 v[46:47], v[46:47], v[42:43]
	v_pk_mul_f32 v[48:49], v[48:49], v[44:45]
	v_pk_mul_f32 v[38:39], v[38:39], v[34:35]
	v_pk_mul_f32 v[40:41], v[40:41], v[36:37]
	v_pk_mul_f32 v[46:47], v[46:47], v[16:17]
	v_pk_mul_f32 v[48:49], v[48:49], v[18:19]
	v_pk_mul_f32 v[38:39], v[38:39], v[20:21]
	v_pk_mul_f32 v[40:41], v[40:41], v[22:23]
	v_cvt_pk_fp8_f32 v10, v46, v47
	v_cvt_pk_fp8_f32 v11, v38, v39
	v_cvt_pk_fp8_f32 v10, v48, v49 op_sel:[0,0,1]
	v_cvt_pk_fp8_f32 v11, v40, v41 op_sel:[0,0,1]
	v_add_u32_e32 v6, 0xa0, v6
	v_mad_i64_i32 v[4:5], s[46:47], v6, s77, v[4:5]
	v_permlane16_swap_b32_e32 v8, v10
	v_permlane16_swap_b32_e32 v9, v11
	v_lshl_add_u64 v[2:3], v[4:5], 0, v[2:3]
	s_andn2_b64 vcc, exec, s[0:1]
	s_mov_b64 s[0:1], -1
	global_store_dwordx4 v[2:3], v[8:11], off
	s_cbranch_vccnz .LBB0_707
	s_andn2_b64 vcc, exec, s[6:7]
	s_cbranch_vccnz .LBB0_706
	s_barrier
	s_branch .LBB0_706

.LBB0_1914:
	v_pk_mul_f32 v[16:17], v[158:159], s[22:23] op_sel_hi:[1,0]
	v_pk_mul_f32 v[18:19], v[160:161], s[22:23] op_sel_hi:[1,0]
	v_pk_mul_f32 v[20:21], v[150:151], s[22:23] op_sel_hi:[1,0]
	v_pk_mul_f32 v[22:23], v[152:153], s[22:23] op_sel_hi:[1,0]
	v_exp_f32_e32 v16, v16
	v_exp_f32_e32 v17, v17
	v_exp_f32_e32 v18, v18
	v_exp_f32_e32 v19, v19
	v_exp_f32_e32 v20, v20
	v_exp_f32_e32 v21, v21
	v_exp_f32_e32 v22, v22
	v_exp_f32_e32 v23, v23
	v_pk_add_f32 v[16:17], v[16:17], 1.0 op_sel_hi:[1,0]
	v_pk_add_f32 v[18:19], v[18:19], 1.0 op_sel_hi:[1,0]
	v_pk_add_f32 v[20:21], v[20:21], 1.0 op_sel_hi:[1,0]
	v_pk_add_f32 v[22:23], v[22:23], 1.0 op_sel_hi:[1,0]
	v_rcp_f32_e32 v16, v16
	v_rcp_f32_e32 v17, v17
	v_rcp_f32_e32 v18, v18
	v_rcp_f32_e32 v19, v19
	v_rcp_f32_e32 v20, v20
	v_rcp_f32_e32 v21, v21
	v_rcp_f32_e32 v22, v22
	v_rcp_f32_e32 v23, v23
	v_pk_mul_f32 v[158:159], v[158:159], v[154:155]
	v_pk_mul_f32 v[160:161], v[160:161], v[156:157]
	v_pk_mul_f32 v[150:151], v[150:151], v[146:147]
	v_pk_mul_f32 v[152:153], v[152:153], v[148:149]
	v_pk_mul_f32 v[158:159], v[158:159], v[16:17]
	v_pk_mul_f32 v[160:161], v[160:161], v[18:19]
	v_pk_mul_f32 v[150:151], v[150:151], v[20:21]
	v_pk_mul_f32 v[152:153], v[152:153], v[22:23]
	v_cvt_pk_fp8_f32 v8, v158, v159
	v_cvt_pk_fp8_f32 v9, v150, v151
	v_cvt_pk_fp8_f32 v8, v160, v161 op_sel:[0,0,1]
	v_cvt_pk_fp8_f32 v9, v152, v153 op_sel:[0,0,1]
	v_pk_mul_f32 v[16:17], v[142:143], s[22:23] op_sel_hi:[1,0]
	v_pk_mul_f32 v[18:19], v[144:145], s[22:23] op_sel_hi:[1,0]
	v_pk_mul_f32 v[20:21], v[134:135], s[22:23] op_sel_hi:[1,0]
	v_pk_mul_f32 v[22:23], v[136:137], s[22:23] op_sel_hi:[1,0]
	v_exp_f32_e32 v16, v16
	v_exp_f32_e32 v17, v17
	v_exp_f32_e32 v18, v18
	v_exp_f32_e32 v19, v19
	v_exp_f32_e32 v20, v20
	v_exp_f32_e32 v21, v21
	v_exp_f32_e32 v22, v22
	v_exp_f32_e32 v23, v23
	v_pk_add_f32 v[16:17], v[16:17], 1.0 op_sel_hi:[1,0]
	v_pk_add_f32 v[18:19], v[18:19], 1.0 op_sel_hi:[1,0]
	v_pk_add_f32 v[20:21], v[20:21], 1.0 op_sel_hi:[1,0]
	v_pk_add_f32 v[22:23], v[22:23], 1.0 op_sel_hi:[1,0]
	v_rcp_f32_e32 v16, v16
	v_rcp_f32_e32 v17, v17
	v_rcp_f32_e32 v18, v18
	v_rcp_f32_e32 v19, v19
	v_rcp_f32_e32 v20, v20
	v_rcp_f32_e32 v21, v21
	v_rcp_f32_e32 v22, v22
	v_rcp_f32_e32 v23, v23
	v_pk_mul_f32 v[142:143], v[142:143], v[138:139]
	v_pk_mul_f32 v[144:145], v[144:145], v[140:141]
	v_pk_mul_f32 v[134:135], v[134:135], v[130:131]
	v_pk_mul_f32 v[136:137], v[136:137], v[132:133]
	v_pk_mul_f32 v[142:143], v[142:143], v[16:17]
	v_pk_mul_f32 v[144:145], v[144:145], v[18:19]
	v_pk_mul_f32 v[134:135], v[134:135], v[20:21]
	v_pk_mul_f32 v[136:137], v[136:137], v[22:23]
	v_cvt_pk_fp8_f32 v10, v142, v143
	v_cvt_pk_fp8_f32 v11, v134, v135
	v_cvt_pk_fp8_f32 v10, v144, v145 op_sel:[0,0,1]
	v_cvt_pk_fp8_f32 v11, v136, v137 op_sel:[0,0,1]
	v_lshl_or_b32 v2, s40, 7, v196
	v_lshl_add_u32 v6, s78, 8, v195
	v_mov_b64_e32 v[4:5], s[14:15]
	v_ashrrev_i32_e32 v3, 31, v2
	v_mad_i64_i32 v[14:15], s[42:43], v6, s67, v[4:5]
	v_permlane16_swap_b32_e32 v8, v10
	v_permlane16_swap_b32_e32 v9, v11
	v_lshl_add_u64 v[14:15], v[14:15], 0, v[2:3]
	global_store_dwordx4 v[14:15], v[8:11], off
	v_pk_mul_f32 v[16:17], v[126:127], s[22:23] op_sel_hi:[1,0]
	v_pk_mul_f32 v[18:19], v[128:129], s[22:23] op_sel_hi:[1,0]
	v_pk_mul_f32 v[20:21], v[118:119], s[22:23] op_sel_hi:[1,0]
	v_pk_mul_f32 v[22:23], v[120:121], s[22:23] op_sel_hi:[1,0]
	v_exp_f32_e32 v16, v16
	v_exp_f32_e32 v17, v17
	v_exp_f32_e32 v18, v18
	v_exp_f32_e32 v19, v19
	v_exp_f32_e32 v20, v20
	v_exp_f32_e32 v21, v21
	v_exp_f32_e32 v22, v22
	v_exp_f32_e32 v23, v23
	v_pk_add_f32 v[16:17], v[16:17], 1.0 op_sel_hi:[1,0]
	v_pk_add_f32 v[18:19], v[18:19], 1.0 op_sel_hi:[1,0]
	v_pk_add_f32 v[20:21], v[20:21], 1.0 op_sel_hi:[1,0]
	v_pk_add_f32 v[22:23], v[22:23], 1.0 op_sel_hi:[1,0]
	v_rcp_f32_e32 v16, v16
	v_rcp_f32_e32 v17, v17
	v_rcp_f32_e32 v18, v18
	v_rcp_f32_e32 v19, v19
	v_rcp_f32_e32 v20, v20
	v_rcp_f32_e32 v21, v21
	v_rcp_f32_e32 v22, v22
	v_rcp_f32_e32 v23, v23
	v_pk_mul_f32 v[126:127], v[126:127], v[122:123]
	v_pk_mul_f32 v[128:129], v[128:129], v[124:125]
	v_pk_mul_f32 v[118:119], v[118:119], v[114:115]
	v_pk_mul_f32 v[120:121], v[120:121], v[116:117]
	v_pk_mul_f32 v[126:127], v[126:127], v[16:17]
	v_pk_mul_f32 v[128:129], v[128:129], v[18:19]
	v_pk_mul_f32 v[118:119], v[118:119], v[20:21]
	v_pk_mul_f32 v[120:121], v[120:121], v[22:23]
	v_cvt_pk_fp8_f32 v8, v126, v127
	v_cvt_pk_fp8_f32 v9, v118, v119
	v_cvt_pk_fp8_f32 v8, v128, v129 op_sel:[0,0,1]
	v_cvt_pk_fp8_f32 v9, v120, v121 op_sel:[0,0,1]
	v_pk_mul_f32 v[16:17], v[110:111], s[22:23] op_sel_hi:[1,0]
	v_pk_mul_f32 v[18:19], v[112:113], s[22:23] op_sel_hi:[1,0]
	v_pk_mul_f32 v[20:21], v[102:103], s[22:23] op_sel_hi:[1,0]
	v_pk_mul_f32 v[22:23], v[104:105], s[22:23] op_sel_hi:[1,0]
	v_exp_f32_e32 v16, v16
	v_exp_f32_e32 v17, v17
	v_exp_f32_e32 v18, v18
	v_exp_f32_e32 v19, v19
	v_exp_f32_e32 v20, v20
	v_exp_f32_e32 v21, v21
	v_exp_f32_e32 v22, v22
	v_exp_f32_e32 v23, v23
	v_pk_add_f32 v[16:17], v[16:17], 1.0 op_sel_hi:[1,0]
	v_pk_add_f32 v[18:19], v[18:19], 1.0 op_sel_hi:[1,0]
	v_pk_add_f32 v[20:21], v[20:21], 1.0 op_sel_hi:[1,0]
	v_pk_add_f32 v[22:23], v[22:23], 1.0 op_sel_hi:[1,0]
	v_rcp_f32_e32 v16, v16
	v_rcp_f32_e32 v17, v17
	v_rcp_f32_e32 v18, v18
	v_rcp_f32_e32 v19, v19
	v_rcp_f32_e32 v20, v20
	v_rcp_f32_e32 v21, v21
	v_rcp_f32_e32 v22, v22
	v_rcp_f32_e32 v23, v23
	v_pk_mul_f32 v[110:111], v[110:111], v[106:107]
	v_pk_mul_f32 v[112:113], v[112:113], v[108:109]
	v_pk_mul_f32 v[102:103], v[102:103], v[98:99]
	v_pk_mul_f32 v[104:105], v[104:105], v[100:101]
	v_pk_mul_f32 v[110:111], v[110:111], v[16:17]
	v_pk_mul_f32 v[112:113], v[112:113], v[18:19]
	v_pk_mul_f32 v[102:103], v[102:103], v[20:21]
	v_pk_mul_f32 v[104:105], v[104:105], v[22:23]
	v_cvt_pk_fp8_f32 v10, v110, v111
	v_cvt_pk_fp8_f32 v11, v102, v103
	v_cvt_pk_fp8_f32 v10, v112, v113 op_sel:[0,0,1]
	v_cvt_pk_fp8_f32 v11, v104, v105 op_sel:[0,0,1]
	v_or_b32_e32 v7, 32, v6
	v_mad_i64_i32 v[12:13], s[42:43], v7, s67, v[4:5]
	v_permlane16_swap_b32_e32 v8, v10
	v_permlane16_swap_b32_e32 v9, v11
	v_lshl_add_u64 v[12:13], v[12:13], 0, v[2:3]
	global_store_dwordx4 v[12:13], v[8:11], off
	v_pk_mul_f32 v[16:17], v[94:95], s[22:23] op_sel_hi:[1,0]
	v_pk_mul_f32 v[18:19], v[96:97], s[22:23] op_sel_hi:[1,0]
	v_pk_mul_f32 v[20:21], v[86:87], s[22:23] op_sel_hi:[1,0]
	v_pk_mul_f32 v[22:23], v[88:89], s[22:23] op_sel_hi:[1,0]
	v_exp_f32_e32 v16, v16
	v_exp_f32_e32 v17, v17
	v_exp_f32_e32 v18, v18
	v_exp_f32_e32 v19, v19
	v_exp_f32_e32 v20, v20
	v_exp_f32_e32 v21, v21
	v_exp_f32_e32 v22, v22
	v_exp_f32_e32 v23, v23
	v_pk_add_f32 v[16:17], v[16:17], 1.0 op_sel_hi:[1,0]
	v_pk_add_f32 v[18:19], v[18:19], 1.0 op_sel_hi:[1,0]
	v_pk_add_f32 v[20:21], v[20:21], 1.0 op_sel_hi:[1,0]
	v_pk_add_f32 v[22:23], v[22:23], 1.0 op_sel_hi:[1,0]
	v_rcp_f32_e32 v16, v16
	v_rcp_f32_e32 v17, v17
	v_rcp_f32_e32 v18, v18
	v_rcp_f32_e32 v19, v19
	v_rcp_f32_e32 v20, v20
	v_rcp_f32_e32 v21, v21
	v_rcp_f32_e32 v22, v22
	v_rcp_f32_e32 v23, v23
	v_pk_mul_f32 v[94:95], v[94:95], v[90:91]
	v_pk_mul_f32 v[96:97], v[96:97], v[92:93]
	v_pk_mul_f32 v[86:87], v[86:87], v[82:83]
	v_pk_mul_f32 v[88:89], v[88:89], v[84:85]
	v_pk_mul_f32 v[94:95], v[94:95], v[16:17]
	v_pk_mul_f32 v[96:97], v[96:97], v[18:19]
	v_pk_mul_f32 v[86:87], v[86:87], v[20:21]
	v_pk_mul_f32 v[88:89], v[88:89], v[22:23]
	v_cvt_pk_fp8_f32 v8, v94, v95
	v_cvt_pk_fp8_f32 v9, v86, v87
	v_cvt_pk_fp8_f32 v8, v96, v97 op_sel:[0,0,1]
	v_cvt_pk_fp8_f32 v9, v88, v89 op_sel:[0,0,1]
	v_pk_mul_f32 v[16:17], v[78:79], s[22:23] op_sel_hi:[1,0]
	v_pk_mul_f32 v[18:19], v[80:81], s[22:23] op_sel_hi:[1,0]
	v_pk_mul_f32 v[20:21], v[70:71], s[22:23] op_sel_hi:[1,0]
	v_pk_mul_f32 v[22:23], v[72:73], s[22:23] op_sel_hi:[1,0]
	v_exp_f32_e32 v16, v16
	v_exp_f32_e32 v17, v17
	v_exp_f32_e32 v18, v18
	v_exp_f32_e32 v19, v19
	v_exp_f32_e32 v20, v20
	v_exp_f32_e32 v21, v21
	v_exp_f32_e32 v22, v22
	v_exp_f32_e32 v23, v23
	v_pk_add_f32 v[16:17], v[16:17], 1.0 op_sel_hi:[1,0]
	v_pk_add_f32 v[18:19], v[18:19], 1.0 op_sel_hi:[1,0]
	v_pk_add_f32 v[20:21], v[20:21], 1.0 op_sel_hi:[1,0]
	v_pk_add_f32 v[22:23], v[22:23], 1.0 op_sel_hi:[1,0]
	v_rcp_f32_e32 v16, v16
	v_rcp_f32_e32 v17, v17
	v_rcp_f32_e32 v18, v18
	v_rcp_f32_e32 v19, v19
	v_rcp_f32_e32 v20, v20
	v_rcp_f32_e32 v21, v21
	v_rcp_f32_e32 v22, v22
	v_rcp_f32_e32 v23, v23
	v_pk_mul_f32 v[78:79], v[78:79], v[74:75]
	v_pk_mul_f32 v[80:81], v[80:81], v[76:77]
	v_pk_mul_f32 v[70:71], v[70:71], v[66:67]
	v_pk_mul_f32 v[72:73], v[72:73], v[68:69]
	v_pk_mul_f32 v[78:79], v[78:79], v[16:17]
	v_pk_mul_f32 v[80:81], v[80:81], v[18:19]
	v_pk_mul_f32 v[70:71], v[70:71], v[20:21]
	v_pk_mul_f32 v[72:73], v[72:73], v[22:23]
	v_cvt_pk_fp8_f32 v10, v78, v79
	v_cvt_pk_fp8_f32 v11, v70, v71
	v_cvt_pk_fp8_f32 v10, v80, v81 op_sel:[0,0,1]
	v_cvt_pk_fp8_f32 v11, v72, v73 op_sel:[0,0,1]
	v_add_u32_e32 v7, 0x80, v6
	v_mad_i64_i32 v[12:13], s[42:43], v7, s67, v[4:5]
	v_permlane16_swap_b32_e32 v8, v10
	v_permlane16_swap_b32_e32 v9, v11
	v_lshl_add_u64 v[12:13], v[12:13], 0, v[2:3]
	global_store_dwordx4 v[12:13], v[8:11], off
	v_pk_mul_f32 v[16:17], v[58:59], s[22:23] op_sel_hi:[1,0]
	v_pk_mul_f32 v[18:19], v[60:61], s[22:23] op_sel_hi:[1,0]
	v_pk_mul_f32 v[20:21], v[46:47], s[22:23] op_sel_hi:[1,0]
	v_pk_mul_f32 v[22:23], v[48:49], s[22:23] op_sel_hi:[1,0]
	v_exp_f32_e32 v16, v16
	v_exp_f32_e32 v17, v17
	v_exp_f32_e32 v18, v18
	v_exp_f32_e32 v19, v19
	v_exp_f32_e32 v20, v20
	v_exp_f32_e32 v21, v21
	v_exp_f32_e32 v22, v22
	v_exp_f32_e32 v23, v23
	v_pk_add_f32 v[16:17], v[16:17], 1.0 op_sel_hi:[1,0]
	v_pk_add_f32 v[18:19], v[18:19], 1.0 op_sel_hi:[1,0]
	v_pk_add_f32 v[20:21], v[20:21], 1.0 op_sel_hi:[1,0]
	v_pk_add_f32 v[22:23], v[22:23], 1.0 op_sel_hi:[1,0]
	v_rcp_f32_e32 v16, v16
	v_rcp_f32_e32 v17, v17
	v_rcp_f32_e32 v18, v18
	v_rcp_f32_e32 v19, v19
	v_rcp_f32_e32 v20, v20
	v_rcp_f32_e32 v21, v21
	v_rcp_f32_e32 v22, v22
	v_rcp_f32_e32 v23, v23
	v_pk_mul_f32 v[58:59], v[58:59], v[50:51]
	v_pk_mul_f32 v[60:61], v[60:61], v[52:53]
	v_pk_mul_f32 v[46:47], v[46:47], v[42:43]
	v_pk_mul_f32 v[48:49], v[48:49], v[44:45]
	v_pk_mul_f32 v[58:59], v[58:59], v[16:17]
	v_pk_mul_f32 v[60:61], v[60:61], v[18:19]
	v_pk_mul_f32 v[46:47], v[46:47], v[20:21]
	v_pk_mul_f32 v[48:49], v[48:49], v[22:23]
	v_cvt_pk_fp8_f32 v8, v58, v59
	v_cvt_pk_fp8_f32 v9, v46, v47
	v_cvt_pk_fp8_f32 v8, v60, v61 op_sel:[0,0,1]
	v_cvt_pk_fp8_f32 v9, v48, v49 op_sel:[0,0,1]
	v_pk_mul_f32 v[16:17], v[38:39], s[22:23] op_sel_hi:[1,0]
	v_pk_mul_f32 v[18:19], v[40:41], s[22:23] op_sel_hi:[1,0]
	v_pk_mul_f32 v[20:21], v[34:35], s[22:23] op_sel_hi:[1,0]
	v_pk_mul_f32 v[22:23], v[36:37], s[22:23] op_sel_hi:[1,0]
	v_exp_f32_e32 v16, v16
	v_exp_f32_e32 v17, v17
	v_exp_f32_e32 v18, v18
	v_exp_f32_e32 v19, v19
	v_exp_f32_e32 v20, v20
	v_exp_f32_e32 v21, v21
	v_exp_f32_e32 v22, v22
	v_exp_f32_e32 v23, v23
	v_pk_add_f32 v[16:17], v[16:17], 1.0 op_sel_hi:[1,0]
	v_pk_add_f32 v[18:19], v[18:19], 1.0 op_sel_hi:[1,0]
	v_pk_add_f32 v[20:21], v[20:21], 1.0 op_sel_hi:[1,0]
	v_pk_add_f32 v[22:23], v[22:23], 1.0 op_sel_hi:[1,0]
	v_rcp_f32_e32 v16, v16
	v_rcp_f32_e32 v17, v17
	v_rcp_f32_e32 v18, v18
	v_rcp_f32_e32 v19, v19
	v_rcp_f32_e32 v20, v20
	v_rcp_f32_e32 v21, v21
	v_rcp_f32_e32 v22, v22
	v_rcp_f32_e32 v23, v23
	v_pk_mul_f32 v[38:39], v[38:39], v[62:63]
	v_pk_mul_f32 v[40:41], v[40:41], v[64:65]
	v_pk_mul_f32 v[34:35], v[34:35], v[54:55]
	v_pk_mul_f32 v[36:37], v[36:37], v[56:57]
	v_pk_mul_f32 v[38:39], v[38:39], v[16:17]
	v_pk_mul_f32 v[40:41], v[40:41], v[18:19]
	v_pk_mul_f32 v[34:35], v[34:35], v[20:21]
	v_pk_mul_f32 v[36:37], v[36:37], v[22:23]
	v_cvt_pk_fp8_f32 v10, v38, v39
	v_cvt_pk_fp8_f32 v11, v34, v35
	v_cvt_pk_fp8_f32 v10, v40, v41 op_sel:[0,0,1]
	v_cvt_pk_fp8_f32 v11, v36, v37 op_sel:[0,0,1]
	v_add_u32_e32 v6, 0xa0, v6
	v_mad_i64_i32 v[4:5], s[42:43], v6, s67, v[4:5]
	v_permlane16_swap_b32_e32 v8, v10
	v_permlane16_swap_b32_e32 v9, v11
	v_lshl_add_u64 v[2:3], v[4:5], 0, v[2:3]
	s_andn2_b64 vcc, exec, s[0:1]
	s_mov_b64 s[0:1], -1
	global_store_dwordx4 v[2:3], v[8:11], off
	s_cbranch_vccnz .LBB0_1903
	s_andn2_b64 vcc, exec, s[12:13]
	s_cbranch_vccnz .LBB0_1902
	s_barrier
	s_branch .LBB0_1902
